# P3 spatial-gating MFMA section rewritten: transposed LDS reads double-buffered one column block ahead, counted vmcnt so the next unit's prefetch stays in flight
# baseline (speedup 1.0000x reference)
.LBB0_780:
	s_cmp_eq_u32 s98, 1
	s_cbranch_scc1 .Lsgu_p
	s_waitcnt vmcnt(0)
	s_branch .Lsgu_c

.Lsgu_c:
	ds_read_b64_tr_b16 v[116:117], v87 offset:0
	ds_read_b64_tr_b16 v[118:119], v88 offset:0
	ds_read_b64_tr_b16 v[120:121], v87 offset:0x2000
	ds_read_b64_tr_b16 v[122:123], v88 offset:0x2000
	ds_read_b64_tr_b16 v[124:125], v87 offset:0x4000
	ds_read_b64_tr_b16 v[126:127], v88 offset:0x4000
	ds_read_b64_tr_b16 v[128:129], v87 offset:0x6000
	ds_read_b64_tr_b16 v[130:131], v88 offset:0x6000
	ds_read_b64_tr_b16 v[132:133], v89 offset:0
	ds_read_b64_tr_b16 v[134:135], v90 offset:0
	ds_read_b64_tr_b16 v[136:137], v89 offset:0x2000
	ds_read_b64_tr_b16 v[138:139], v90 offset:0x2000
	ds_read_b64_tr_b16 v[140:141], v89 offset:0x4000
	ds_read_b64_tr_b16 v[142:143], v90 offset:0x4000
	ds_read_b64_tr_b16 v[144:145], v89 offset:0x6000
	ds_read_b64_tr_b16 v[146:147], v90 offset:0x6000
	v_lshlrev_b64 v[108:109], 11, v[82:83]
	s_mov_b32 s15, s14
	s_and_b64 vcc, exec, s[6:7]
	s_waitcnt lgkmcnt(8)
	v_mfma_f32_16x16x32_bf16 v[148:151], v[116:119], v[8:11], 0
	v_mfma_f32_16x16x32_bf16 v[148:151], v[120:123], v[0:3], v[148:151]
	v_mfma_f32_16x16x32_bf16 v[148:151], v[124:127], v[4:7], v[148:151]
	v_mfma_f32_16x16x32_bf16 v[148:151], v[128:131], v[12:15], v[148:151]
	ds_read_b64_tr_b16 v[116:117], v91 offset:0
	ds_read_b64_tr_b16 v[118:119], v92 offset:0
	ds_read_b64_tr_b16 v[120:121], v91 offset:0x2000
	ds_read_b64_tr_b16 v[122:123], v92 offset:0x2000
	ds_read_b64_tr_b16 v[124:125], v91 offset:0x4000
	ds_read_b64_tr_b16 v[126:127], v92 offset:0x4000
	ds_read_b64_tr_b16 v[128:129], v91 offset:0x6000
	ds_read_b64_tr_b16 v[130:131], v92 offset:0x6000
	s_waitcnt lgkmcnt(8)
	v_mfma_f32_16x16x32_bf16 v[152:155], v[132:135], v[8:11], 0
	v_mfma_f32_16x16x32_bf16 v[152:155], v[136:139], v[0:3], v[152:155]
	v_mfma_f32_16x16x32_bf16 v[152:155], v[140:143], v[4:7], v[152:155]
	v_mfma_f32_16x16x32_bf16 v[152:155], v[144:147], v[12:15], v[152:155]
	v_lshlrev_b32_e32 v156, 16, v80
	v_and_b32_e32 v157, 0xffff0000, v80
	v_lshlrev_b32_e32 v158, 16, v81
	v_and_b32_e32 v159, 0xffff0000, v81
	v_add_f32_e32 v160, v85, v148
	v_add_f32_e32 v161, v85, v149
	v_add_f32_e32 v162, v85, v150
	v_add_f32_e32 v163, v85, v151
	v_mul_f32_e32 v160, v160, v156
	v_mul_f32_e32 v161, v161, v157
	v_mul_f32_e32 v162, v162, v158
	v_mul_f32_e32 v163, v163, v159
	v_cvt_pk_bf16_f32 v164, v160, v161
	v_cvt_pk_bf16_f32 v165, v162, v163
	v_lshl_add_u64 v[168:169], v[62:63], 0, v[108:109]
	global_store_dwordx2 v[168:169], v[164:165], off
	ds_read_b64_tr_b16 v[132:133], v93 offset:0
	ds_read_b64_tr_b16 v[134:135], v94 offset:0
	ds_read_b64_tr_b16 v[136:137], v93 offset:0x2000
	ds_read_b64_tr_b16 v[138:139], v94 offset:0x2000
	ds_read_b64_tr_b16 v[140:141], v93 offset:0x4000
	ds_read_b64_tr_b16 v[142:143], v94 offset:0x4000
	ds_read_b64_tr_b16 v[144:145], v93 offset:0x6000
	ds_read_b64_tr_b16 v[146:147], v94 offset:0x6000
	s_waitcnt lgkmcnt(8)
	v_mfma_f32_16x16x32_bf16 v[148:151], v[116:119], v[8:11], 0
	v_mfma_f32_16x16x32_bf16 v[148:151], v[120:123], v[0:3], v[148:151]
	v_mfma_f32_16x16x32_bf16 v[148:151], v[124:127], v[4:7], v[148:151]
	v_mfma_f32_16x16x32_bf16 v[148:151], v[128:131], v[12:15], v[148:151]
	v_lshlrev_b32_e32 v156, 16, v78
	v_and_b32_e32 v157, 0xffff0000, v78
	v_lshlrev_b32_e32 v158, 16, v79
	v_and_b32_e32 v159, 0xffff0000, v79
	v_add_f32_e32 v160, v85, v152
	v_add_f32_e32 v161, v85, v153
	v_add_f32_e32 v162, v85, v154
	v_add_f32_e32 v163, v85, v155
	v_mul_f32_e32 v160, v160, v156
	v_mul_f32_e32 v161, v161, v157
	v_mul_f32_e32 v162, v162, v158
	v_mul_f32_e32 v163, v163, v159
	v_cvt_pk_bf16_f32 v166, v160, v161
	v_cvt_pk_bf16_f32 v167, v162, v163
	v_lshl_add_u64 v[170:171], v[60:61], 0, v[108:109]
	v_add_co_u32_e64 v170, s[16:17], s12, v170
	v_addc_co_u32_e64 v171, s[16:17], 0, v171, s[16:17]
	global_store_dwordx2 v[170:171], v[166:167], off offset:32
	ds_read_b64_tr_b16 v[116:117], v95 offset:0
	ds_read_b64_tr_b16 v[118:119], v96 offset:0
	ds_read_b64_tr_b16 v[120:121], v95 offset:0x2000
	ds_read_b64_tr_b16 v[122:123], v96 offset:0x2000
	ds_read_b64_tr_b16 v[124:125], v95 offset:0x4000
	ds_read_b64_tr_b16 v[126:127], v96 offset:0x4000
	ds_read_b64_tr_b16 v[128:129], v95 offset:0x6000
	ds_read_b64_tr_b16 v[130:131], v96 offset:0x6000
	s_waitcnt lgkmcnt(8)
	v_mfma_f32_16x16x32_bf16 v[152:155], v[132:135], v[8:11], 0
	v_mfma_f32_16x16x32_bf16 v[152:155], v[136:139], v[0:3], v[152:155]
	v_mfma_f32_16x16x32_bf16 v[152:155], v[140:143], v[4:7], v[152:155]
	v_mfma_f32_16x16x32_bf16 v[152:155], v[144:147], v[12:15], v[152:155]
	v_lshlrev_b32_e32 v156, 16, v76
	v_and_b32_e32 v157, 0xffff0000, v76
	v_lshlrev_b32_e32 v158, 16, v77
	v_and_b32_e32 v159, 0xffff0000, v77
	v_add_f32_e32 v160, v85, v148
	v_add_f32_e32 v161, v85, v149
	v_add_f32_e32 v162, v85, v150
	v_add_f32_e32 v163, v85, v151
	v_mul_f32_e32 v160, v160, v156
	v_mul_f32_e32 v161, v161, v157
	v_mul_f32_e32 v162, v162, v158
	v_mul_f32_e32 v163, v163, v159
	v_cvt_pk_bf16_f32 v164, v160, v161
	v_cvt_pk_bf16_f32 v165, v162, v163
	global_store_dwordx2 v[170:171], v[164:165], off offset:64
	ds_read_b64_tr_b16 v[132:133], v97 offset:0
	ds_read_b64_tr_b16 v[134:135], v98 offset:0
	ds_read_b64_tr_b16 v[136:137], v97 offset:0x2000
	ds_read_b64_tr_b16 v[138:139], v98 offset:0x2000
	ds_read_b64_tr_b16 v[140:141], v97 offset:0x4000
	ds_read_b64_tr_b16 v[142:143], v98 offset:0x4000
	ds_read_b64_tr_b16 v[144:145], v97 offset:0x6000
	ds_read_b64_tr_b16 v[146:147], v98 offset:0x6000
	s_waitcnt lgkmcnt(8)
	v_mfma_f32_16x16x32_bf16 v[148:151], v[116:119], v[8:11], 0
	v_mfma_f32_16x16x32_bf16 v[148:151], v[120:123], v[0:3], v[148:151]
	v_mfma_f32_16x16x32_bf16 v[148:151], v[124:127], v[4:7], v[148:151]
	v_mfma_f32_16x16x32_bf16 v[148:151], v[128:131], v[12:15], v[148:151]
	v_lshlrev_b32_e32 v156, 16, v74
	v_and_b32_e32 v157, 0xffff0000, v74
	v_lshlrev_b32_e32 v158, 16, v75
	v_and_b32_e32 v159, 0xffff0000, v75
	v_add_f32_e32 v160, v85, v152
	v_add_f32_e32 v161, v85, v153
	v_add_f32_e32 v162, v85, v154
	v_add_f32_e32 v163, v85, v155
	v_mul_f32_e32 v160, v160, v156
	v_mul_f32_e32 v161, v161, v157
	v_mul_f32_e32 v162, v162, v158
	v_mul_f32_e32 v163, v163, v159
	v_cvt_pk_bf16_f32 v166, v160, v161
	v_cvt_pk_bf16_f32 v167, v162, v163
	global_store_dwordx2 v[170:171], v[166:167], off offset:96
	ds_read_b64_tr_b16 v[116:117], v99 offset:0
	ds_read_b64_tr_b16 v[118:119], v100 offset:0
	ds_read_b64_tr_b16 v[120:121], v99 offset:0x2000
	ds_read_b64_tr_b16 v[122:123], v100 offset:0x2000
	ds_read_b64_tr_b16 v[124:125], v99 offset:0x4000
	ds_read_b64_tr_b16 v[126:127], v100 offset:0x4000
	ds_read_b64_tr_b16 v[128:129], v99 offset:0x6000
	ds_read_b64_tr_b16 v[130:131], v100 offset:0x6000
	s_waitcnt lgkmcnt(8)
	v_mfma_f32_16x16x32_bf16 v[152:155], v[132:135], v[8:11], 0
	v_mfma_f32_16x16x32_bf16 v[152:155], v[136:139], v[0:3], v[152:155]
	v_mfma_f32_16x16x32_bf16 v[152:155], v[140:143], v[4:7], v[152:155]
	v_mfma_f32_16x16x32_bf16 v[152:155], v[144:147], v[12:15], v[152:155]
	v_lshlrev_b32_e32 v156, 16, v72
	v_and_b32_e32 v157, 0xffff0000, v72
	v_lshlrev_b32_e32 v158, 16, v73
	v_and_b32_e32 v159, 0xffff0000, v73
	v_add_f32_e32 v160, v85, v148
	v_add_f32_e32 v161, v85, v149
	v_add_f32_e32 v162, v85, v150
	v_add_f32_e32 v163, v85, v151
	v_mul_f32_e32 v160, v160, v156
	v_mul_f32_e32 v161, v161, v157
	v_mul_f32_e32 v162, v162, v158
	v_mul_f32_e32 v163, v163, v159
	v_cvt_pk_bf16_f32 v164, v160, v161
	v_cvt_pk_bf16_f32 v165, v162, v163
	global_store_dwordx2 v[170:171], v[164:165], off offset:128
	ds_read_b64_tr_b16 v[132:133], v101 offset:0
	ds_read_b64_tr_b16 v[134:135], v102 offset:0
	ds_read_b64_tr_b16 v[136:137], v101 offset:0x2000
	ds_read_b64_tr_b16 v[138:139], v102 offset:0x2000
	ds_read_b64_tr_b16 v[140:141], v101 offset:0x4000
	ds_read_b64_tr_b16 v[142:143], v102 offset:0x4000
	ds_read_b64_tr_b16 v[144:145], v101 offset:0x6000
	ds_read_b64_tr_b16 v[146:147], v102 offset:0x6000
	s_waitcnt lgkmcnt(8)
	v_mfma_f32_16x16x32_bf16 v[148:151], v[116:119], v[8:11], 0
	v_mfma_f32_16x16x32_bf16 v[148:151], v[120:123], v[0:3], v[148:151]
	v_mfma_f32_16x16x32_bf16 v[148:151], v[124:127], v[4:7], v[148:151]
	v_mfma_f32_16x16x32_bf16 v[148:151], v[128:131], v[12:15], v[148:151]
	v_lshlrev_b32_e32 v156, 16, v70
	v_and_b32_e32 v157, 0xffff0000, v70
	v_lshlrev_b32_e32 v158, 16, v71
	v_and_b32_e32 v159, 0xffff0000, v71
	v_add_f32_e32 v160, v85, v152
	v_add_f32_e32 v161, v85, v153
	v_add_f32_e32 v162, v85, v154
	v_add_f32_e32 v163, v85, v155
	v_mul_f32_e32 v160, v160, v156
	v_mul_f32_e32 v161, v161, v157
	v_mul_f32_e32 v162, v162, v158
	v_mul_f32_e32 v163, v163, v159
	v_cvt_pk_bf16_f32 v166, v160, v161
	v_cvt_pk_bf16_f32 v167, v162, v163
	global_store_dwordx2 v[170:171], v[166:167], off offset:160
	s_waitcnt lgkmcnt(0)
	v_mfma_f32_16x16x32_bf16 v[152:155], v[132:135], v[8:11], 0
	v_mfma_f32_16x16x32_bf16 v[152:155], v[136:139], v[0:3], v[152:155]
	v_mfma_f32_16x16x32_bf16 v[152:155], v[140:143], v[4:7], v[152:155]
	v_mfma_f32_16x16x32_bf16 v[152:155], v[144:147], v[12:15], v[152:155]
	v_lshlrev_b32_e32 v156, 16, v68
	v_and_b32_e32 v157, 0xffff0000, v68
	v_lshlrev_b32_e32 v158, 16, v69
	v_and_b32_e32 v159, 0xffff0000, v69
	v_add_f32_e32 v160, v85, v148
	v_add_f32_e32 v161, v85, v149
	v_add_f32_e32 v162, v85, v150
	v_add_f32_e32 v163, v85, v151
	v_mul_f32_e32 v160, v160, v156
	v_mul_f32_e32 v161, v161, v157
	v_mul_f32_e32 v162, v162, v158
	v_mul_f32_e32 v163, v163, v159
	v_cvt_pk_bf16_f32 v164, v160, v161
	v_cvt_pk_bf16_f32 v165, v162, v163
	global_store_dwordx2 v[170:171], v[164:165], off offset:192
	v_lshlrev_b32_e32 v156, 16, v66
	v_and_b32_e32 v157, 0xffff0000, v66
	v_lshlrev_b32_e32 v158, 16, v67
	v_and_b32_e32 v159, 0xffff0000, v67
	s_nop 3
	v_add_f32_e32 v160, v85, v152
	v_add_f32_e32 v161, v85, v153
	v_add_f32_e32 v162, v85, v154
	v_add_f32_e32 v163, v85, v155
	v_mul_f32_e32 v160, v160, v156
	v_mul_f32_e32 v161, v161, v157
	v_mul_f32_e32 v162, v162, v158
	v_mul_f32_e32 v163, v163, v159
	v_cvt_pk_bf16_f32 v166, v160, v161
	v_cvt_pk_bf16_f32 v167, v162, v163
	global_store_dwordx2 v[170:171], v[166:167], off offset:224
	s_barrier
	s_cbranch_vccnz .LBB0_785

.LBB0_783:
	s_mov_b32 s98, 0
	s_andn2_b64 vcc, exec, s[8:9]
	s_cbranch_vccnz .LBB0_780
	s_add_i32 s14, s11, s15
	s_and_b32 s8, s14, 0xffffff80
	v_add_u32_e32 v44, s8, v49
	v_ashrrev_i32_e32 v45, 31, v44
	v_readlane_b32 s16, v251, 10
	v_lshlrev_b64 v[32:33], 12, v[44:45]
	v_readlane_b32 s18, v251, 12
	v_readlane_b32 s19, v251, 13
	v_readlane_b32 s17, v251, 11
	s_nop 0
	v_lshl_add_u64 v[32:33], s[18:19], 0, v[32:33]
	v_lshl_add_u64 v[32:33], v[32:33], 0, s[0:1]
	v_lshl_add_u64 v[32:33], v[32:33], 0, v[50:51]
	v_add_co_u32_e32 v36, vcc, 0x40c00000, v32
	v_lshlrev_b32_e32 v32, 1, v44
	s_nop 0
	v_addc_co_u32_e32 v37, vcc, 0, v33, vcc
	v_ashrrev_i32_e32 v33, 31, v32
	v_lshl_add_u64 v[38:39], v[32:33], 2, s[4:5]
	global_load_dwordx4 v[32:35], v[36:37], off offset:2048
	global_load_dwordx2 v[52:53], v[38:39], off
	v_add_u32_e32 v36, 32, v44
	v_ashrrev_i32_e32 v37, 31, v36
	v_lshlrev_b64 v[38:39], 12, v[36:37]
	v_lshl_add_u64 v[38:39], s[18:19], 0, v[38:39]
	v_lshl_add_u64 v[38:39], v[38:39], 0, s[0:1]
	v_lshl_add_u64 v[38:39], v[38:39], 0, v[50:51]
	v_add_co_u32_e32 v40, vcc, s10, v38
	v_lshlrev_b32_e32 v36, 1, v36
	s_nop 0
	v_addc_co_u32_e32 v41, vcc, 0, v39, vcc
	v_ashrrev_i32_e32 v37, 31, v36
	v_lshl_add_u64 v[42:43], v[36:37], 2, s[4:5]
	global_load_dwordx4 v[36:39], v[40:41], off offset:2048
	global_load_dwordx2 v[54:55], v[42:43], off
	v_add_u32_e32 v40, 64, v44
	v_ashrrev_i32_e32 v41, 31, v40
	v_lshlrev_b64 v[42:43], 12, v[40:41]
	v_lshl_add_u64 v[42:43], s[18:19], 0, v[42:43]
	v_lshl_add_u64 v[42:43], v[42:43], 0, s[0:1]
	v_lshl_add_u64 v[42:43], v[42:43], 0, v[50:51]
	v_add_co_u32_e32 v46, vcc, s10, v42
	v_lshlrev_b32_e32 v40, 1, v40
	v_add_u32_e32 v44, 0x60, v44
	v_addc_co_u32_e32 v47, vcc, 0, v43, vcc
	v_ashrrev_i32_e32 v41, 31, v40
	v_ashrrev_i32_e32 v45, 31, v44
	v_lshl_add_u64 v[64:65], v[40:41], 2, s[4:5]
	global_load_dwordx4 v[40:43], v[46:47], off offset:2048
	global_load_dwordx2 v[56:57], v[64:65], off
	v_lshlrev_b64 v[46:47], 12, v[44:45]
	v_lshl_add_u64 v[46:47], s[18:19], 0, v[46:47]
	v_lshl_add_u64 v[46:47], v[46:47], 0, s[0:1]
	v_lshl_add_u64 v[46:47], v[46:47], 0, v[50:51]
	v_add_co_u32_e32 v104, vcc, s10, v46
	v_lshlrev_b32_e32 v44, 1, v44
	s_nop 0
	v_addc_co_u32_e32 v105, vcc, 0, v47, vcc
	v_ashrrev_i32_e32 v45, 31, v44
	v_lshl_add_u64 v[106:107], v[44:45], 2, s[4:5]
	global_load_dwordx4 v[44:47], v[104:105], off offset:2048
	global_load_dwordx2 v[64:65], v[106:107], off
	s_mov_b32 s98, 1
	s_branch .LBB0_780
